# MLA softmax segment trim: K LDS-DMA in saddr form, pads dropped, rare-path scalars, dead branch logic; on top of v034
# speedup vs baseline: 1.0094x; 1.0094x over previous
; #define SBAR() __builtin_amdgcn_sched_barrier(0)
; #define PK4(P, BASE, OUT) do { u32x4 w = {cvtpk(P[BASE + 0], P[BASE + 1]), cvtpk(P[BASE + 2], P[BASE + 3]), cvtpk(P[BASE + 4], P[BASE + 5]), cvtpk(P[BASE + 6], P[BASE + 7])}; \
;     OUT = *reinterpret_cast<bf16x8*>(&w); } while (0)
; __device__ __forceinline__ void smax_tile(f32x16& p0, f32x16& p1, float& mhat, float& l_reg, f32x16 (&o)[4], float* al_l, const bool first, int r32, int hi,
;                                           bf16x8& pa0, bf16x8& pa1, bf16x8& pa2, bf16x8& pa3) {
;     ...
; #pragma unroll
;     for (int r = 0; r < 16; ++r) p0[r] = __builtin_amdgcn_exp2f(p0[r]);
; #pragma unroll
;     for (int r = 0; r < 16; ++r) p1[r] = __builtin_amdgcn_exp2f(p1[r]);
;     float ps = p0[0];
; #pragma unroll
;     for (int r = 1; r < 16; ++r) ps += p0[r];
; #pragma unroll
;     for (int r = 0; r < 16; ++r) ps += p1[r];
;     { auto rr = __builtin_amdgcn_permlane32_swap(__float_as_uint(ps), __float_as_uint(ps), false, false); ps = __uint_as_float(rr[0]) + __uint_as_float(rr[1]); }
;     l_reg += ps;
;     ...
;     PK4(p0, 0, pa0); PK4(p0, 8, pa1); PK4(p1, 0, pa2); PK4(p1, 8, pa3);
; template <int DQK, bool HASQK, bool HASPV>
; __device__ __forceinline__ void seg_m2(const int (&ka_)[4], int vb_, const bf16x8* qr, f32x16& p0, f32x16& p1, const float nm, f32x16 (&o)[4], bf16x8 pa0, bf16x8 pa1, bf16x8 pa2, bf16x8 pa3) {
;     ...
;     slot_read<DQK, HASQK, HASPV, 0>(kf, vf, ka_, vb_); slot_read<DQK, HASQK, HASPV, 1>(kf, vf, ka_, vb_); slot_read<DQK, HASQK, HASPV, 2>(kf, vf, ka_, vb_); slot_read<DQK, HASQK, HASPV, 3>(kf, vf, ka_, vb_);
;     SBAR();
;     f32x16 negm;
; #pragma unroll
;     for (int r = 0; r < 16; ++r) negm[r] = nm;
;     asm volatile("" : "+v"(negm));
;     SBAR();
.LBB0_605:
	v_exp_f32_e32 v96, v96
	v_exp_f32_e32 v97, v97
	v_exp_f32_e32 v98, v98
	v_exp_f32_e32 v99, v99
	v_exp_f32_e32 v100, v100
	v_exp_f32_e32 v101, v101
	v_add_f32_e32 v160, v96, v97
	v_exp_f32_e32 v102, v102
	v_add_f32_e32 v160, v98, v160
	v_exp_f32_e32 v103, v103
	v_add_f32_e32 v160, v99, v160
	v_exp_f32_e32 v104, v104
	v_add_f32_e32 v160, v100, v160
	v_exp_f32_e32 v105, v105
	v_add_f32_e32 v160, v101, v160
	v_exp_f32_e32 v106, v106
	v_add_f32_e32 v160, v102, v160
	v_exp_f32_e32 v107, v107
	v_add_f32_e32 v160, v103, v160
	v_exp_f32_e32 v108, v108
	v_add_f32_e32 v160, v104, v160
	v_exp_f32_e32 v109, v109
	v_add_f32_e32 v160, v105, v160
	v_exp_f32_e32 v110, v110
	v_add_f32_e32 v160, v106, v160
	v_exp_f32_e32 v111, v111
	v_add_f32_e32 v160, v107, v160
	v_exp_f32_e32 v80, v80
	v_add_f32_e32 v160, v108, v160
	v_exp_f32_e32 v81, v81
	v_add_f32_e32 v160, v109, v160
	v_exp_f32_e32 v82, v82
	v_add_f32_e32 v160, v110, v160
	v_exp_f32_e32 v83, v83
	v_add_f32_e32 v160, v111, v160
	v_exp_f32_e32 v84, v84
	v_add_f32_e32 v160, v80, v160
	v_exp_f32_e32 v85, v85
	v_add_f32_e32 v160, v81, v160
	v_exp_f32_e32 v86, v86
	v_add_f32_e32 v160, v82, v160
	v_exp_f32_e32 v87, v87
	v_add_f32_e32 v160, v83, v160
	v_exp_f32_e32 v88, v88
	v_add_f32_e32 v160, v84, v160
	v_exp_f32_e32 v89, v89
	v_add_f32_e32 v160, v85, v160
	v_exp_f32_e32 v90, v90
	v_add_f32_e32 v160, v86, v160
	v_exp_f32_e32 v91, v91
	v_add_f32_e32 v160, v87, v160
	v_exp_f32_e32 v92, v92
	v_add_f32_e32 v160, v88, v160
	v_exp_f32_e32 v93, v93
	v_add_f32_e32 v160, v89, v160
	v_exp_f32_e32 v94, v94
	v_add_f32_e32 v160, v90, v160
	v_exp_f32_e32 v95, v95
	v_add_f32_e32 v160, v91, v160
	v_add_f32_e32 v160, v92, v160
	v_add_f32_e32 v160, v93, v160
	v_add_f32_e32 v160, v94, v160
	v_add_f32_e32 v160, v95, v160
	v_mov_b32_e32 v161, v160
	v_cvt_pk_bf16_f32 v172, v96, v97
	v_cvt_pk_bf16_f32 v173, v98, v99
	v_permlane32_swap_b32_e32 v160, v161
	v_add_f32_e32 v160, v160, v161
	v_add_f32_e32 v204, v204, v160
	v_cvt_pk_bf16_f32 v174, v100, v101
	v_cvt_pk_bf16_f32 v175, v102, v103
	v_cvt_pk_bf16_f32 v168, v104, v105
	v_cvt_pk_bf16_f32 v169, v106, v107
	v_cvt_pk_bf16_f32 v170, v108, v109
	v_cvt_pk_bf16_f32 v171, v110, v111
	v_cvt_pk_bf16_f32 v164, v80, v81
	v_cvt_pk_bf16_f32 v165, v82, v83
	v_cvt_pk_bf16_f32 v166, v84, v85
	v_cvt_pk_bf16_f32 v167, v86, v87
	v_cvt_pk_bf16_f32 v160, v88, v89
	v_cvt_pk_bf16_f32 v161, v90, v91
	v_cvt_pk_bf16_f32 v162, v92, v93
	v_cvt_pk_bf16_f32 v163, v94, v95
	s_mul_i32 s47, s26, 0x6000
	s_addk_i32 s93, 0xc000
	s_cmp_lg_u32 s26, 0
	s_cselect_b32 s46, s93, 0x8000
	v_add_u32_e32 v227, s46, v202
	v_add_u32_e32 v207, s47, v185
	v_add_u32_e32 v224, s47, v187
	v_add_u32_e32 v225, s47, v205
	v_add_u32_e32 v226, s47, v206
	s_waitcnt lgkmcnt(0)
	ds_read_b64_tr_b16 v[208:209], v227 offset:0
	ds_read_b64_tr_b16 v[210:211], v227 offset:2048
	ds_read_b64_tr_b16 v[212:213], v227 offset:512
	ds_read_b64_tr_b16 v[214:215], v227 offset:2560
	ds_read_b64_tr_b16 v[216:217], v227 offset:1024
	ds_read_b64_tr_b16 v[218:219], v227 offset:3072
	ds_read_b64_tr_b16 v[220:221], v227 offset:1536
	ds_read_b64_tr_b16 v[222:223], v227 offset:3584
	s_barrier
	s_waitcnt lgkmcnt(6)
	v_mfma_f32_32x32x16_bf16 v[64:79], v[172:175], v[208:211], v[64:79]
	ds_read_b64_tr_b16 v[208:209], v227 offset:4096
	ds_read_b64_tr_b16 v[210:211], v227 offset:6144
	s_waitcnt lgkmcnt(6)
	v_mfma_f32_32x32x16_bf16 v[48:63], v[172:175], v[212:215], v[48:63]
	ds_read_b64_tr_b16 v[212:213], v227 offset:4608
	ds_read_b64_tr_b16 v[214:215], v227 offset:6656
	s_waitcnt lgkmcnt(6)
	v_mfma_f32_32x32x16_bf16 v[32:47], v[172:175], v[216:219], v[32:47]
	ds_read_b64_tr_b16 v[216:217], v227 offset:5120
	ds_read_b64_tr_b16 v[218:219], v227 offset:7168
	s_waitcnt lgkmcnt(6)
	v_mfma_f32_32x32x16_bf16 v[16:31], v[172:175], v[220:223], v[16:31]
	ds_read_b64_tr_b16 v[220:221], v227 offset:5632
	ds_read_b64_tr_b16 v[222:223], v227 offset:7680
	s_waitcnt lgkmcnt(6)
	v_mfma_f32_32x32x16_bf16 v[64:79], v[168:171], v[208:211], v[64:79]
	ds_read_b64_tr_b16 v[208:209], v227 offset:8192
	ds_read_b64_tr_b16 v[210:211], v227 offset:10240
	s_waitcnt lgkmcnt(6)
	v_mfma_f32_32x32x16_bf16 v[48:63], v[168:171], v[212:215], v[48:63]
	ds_read_b64_tr_b16 v[212:213], v227 offset:8704
	ds_read_b64_tr_b16 v[214:215], v227 offset:10752
	s_waitcnt lgkmcnt(6)
	v_mfma_f32_32x32x16_bf16 v[32:47], v[168:171], v[216:219], v[32:47]
	ds_read_b64_tr_b16 v[216:217], v227 offset:9216
	ds_read_b64_tr_b16 v[218:219], v227 offset:11264
	s_waitcnt lgkmcnt(6)
	v_mfma_f32_32x32x16_bf16 v[16:31], v[168:171], v[220:223], v[16:31]
	ds_read_b64_tr_b16 v[220:221], v227 offset:9728
	ds_read_b64_tr_b16 v[222:223], v227 offset:11776
	s_waitcnt lgkmcnt(6)
	v_mfma_f32_32x32x16_bf16 v[64:79], v[164:167], v[208:211], v[64:79]
	ds_read_b64_tr_b16 v[208:209], v227 offset:12288
	ds_read_b64_tr_b16 v[210:211], v227 offset:14336
	s_waitcnt lgkmcnt(6)
	v_mfma_f32_32x32x16_bf16 v[48:63], v[164:167], v[212:215], v[48:63]
	ds_read_b64_tr_b16 v[212:213], v227 offset:12800
	ds_read_b64_tr_b16 v[214:215], v227 offset:14848
	s_waitcnt lgkmcnt(6)
	v_mfma_f32_32x32x16_bf16 v[32:47], v[164:167], v[216:219], v[32:47]
	ds_read_b64_tr_b16 v[216:217], v227 offset:13312
	ds_read_b64_tr_b16 v[218:219], v227 offset:15360
	s_waitcnt lgkmcnt(6)
	v_mfma_f32_32x32x16_bf16 v[16:31], v[164:167], v[220:223], v[16:31]
	ds_read_b64_tr_b16 v[220:221], v227 offset:13824
	ds_read_b64_tr_b16 v[222:223], v227 offset:15872
	v_xor_b32_e32 v80, 0x80000000, v203
	v_mov_b32_e32 v81, v80
	v_mov_b32_e32 v82, v80
	v_mov_b32_e32 v83, v80
	v_mov_b32_e32 v84, v80
	v_mov_b32_e32 v85, v80
	v_mov_b32_e32 v86, v80
	v_mov_b32_e32 v87, v80
	v_mov_b32_e32 v88, v80
	v_mov_b32_e32 v89, v80
	v_mov_b32_e32 v90, v80
	v_mov_b32_e32 v91, v80
	v_mov_b32_e32 v92, v80
	v_mov_b32_e32 v93, v80
	v_mov_b32_e32 v94, v80
	v_mov_b32_e32 v95, v80
	s_waitcnt lgkmcnt(6)
; #define SBAR() __builtin_amdgcn_sched_barrier(0)
; template <int OFF> __device__ __forceinline__ void dsr128(bf16x8& d, int addr) { asm volatile("ds_read_b128 %0, %1 offset:%2" : "=v"(d) : "v"(addr), "i"(OFF)); }
; template <int OFF> __device__ __forceinline__ void dstr64(s16x4& d, int addr) { asm volatile("ds_read_b64_tr_b16 %0, %1 offset:%2" : "=v"(d) : "v"(addr), "i"(OFF)); }
; template <int DQK, bool HASQK, bool HASPV, int J>
; __device__ __forceinline__ void slot_read(bf16x8 (&kf)[DQK / 16][2], s16x4 (&vf)[4][8], const int (&ka_)[4], int vb_) {
;     constexpr int NQS = HASQK ? 2 * (DQK / 16) : 0, NS = NQS + (HASPV ? 16 : 0);
;     if constexpr (J < NQS) { constexpr int d0 = J >> 1, h = J & 1; dsr128<(d0 >> 2) * 128 + h * 32 * DQK * 2>(kf[d0][h], ka_[d0 & 3]); }
;     else if constexpr (J < NS) { constexpr int q = J - NQS, g = q >> 2, d = q & 3; dstr64<v_rd_off(d, g, 0)>(vf[g][2 * d], vb_); dstr64<v_rd_off(d, g, 1)>(vf[g][2 * d + 1], vb_); }
; }
; template <int DQK, bool HASQK, bool HASPV, int J> ...
;     constexpr int NQS = HASQK ? 2 * (DQK / 16) : 0, NS = NQS + (HASPV ? 16 : 0);
;     if constexpr (J < NS) {
;         constexpr int rd1 = (J + 1 < NS) ? ((J + 1 < NQS) ? 1 : 2) : 0, rd2 = (J + 2 < NS) ? ((J + 2 < NQS) ? 1 : 2) : 0, rd3 = (J + 3 < NS) ? ((J + 3 < NQS) ? 1 : 2) : 0, NW = rd1 + rd2 + rd3;
;     ...
;         if constexpr (J < NQS) { constexpr int d0 = J >> 1, h = J & 1;
;             LWN1(kf[d0][h]); SBAR();
;             if constexpr (h == 0) p0 = __builtin_amdgcn_mfma_f32_32x32x16_bf16(kf[d0][0], qr[d0], (d0 == 0) ? negm : p0, 0, 0, 0);
;             else p1 = __builtin_amdgcn_mfma_f32_32x32x16_bf16(kf[d0][1], qr[d0], (d0 == 0) ? negm : p1, 0, 0, 0);
;         } else { constexpr int q = J - NQS, g = q >> 2, d = q & 3;
;             LWN2(vf[g][2 * d], vf[g][2 * d + 1]); SBAR();
;             o[d] = __builtin_amdgcn_mfma_f32_32x32x16_bf16(pa[g], (bf16x8){vf[g][2 * d][0], vf[g][2 * d][1], vf[g][2 * d][2], vf[g][2 * d][3], vf[g][2 * d + 1][0], vf[g][2 * d + 1][1], vf[g][2 * d + 1][2], vf[g][2 * d + 1][3]}, o[d], 0, 0, 0);
;         }
;     ...
;         SBAR();
;         slot_read<DQK, HASQK, HASPV, J + 4>(kf, vf, ka_, vb_);
;         SBAR();
;         slot_run<DQK, HASQK, HASPV, J + 1>(kf, vf, ka_, vb_, qr, p0, p1, negm, o, pa);
;     }
; }
	v_mfma_f32_32x32x16_bf16 v[64:79], v[160:163], v[208:211], v[64:79]
	ds_read_b128 v[208:211], v207 offset:0
	s_waitcnt lgkmcnt(5)
	v_mfma_f32_32x32x16_bf16 v[48:63], v[160:163], v[212:215], v[48:63]
	ds_read_b128 v[212:215], v207 offset:12288
	s_waitcnt lgkmcnt(4)
	v_mfma_f32_32x32x16_bf16 v[32:47], v[160:163], v[216:219], v[32:47]
	ds_read_b128 v[216:219], v224 offset:0
	s_waitcnt lgkmcnt(3)
	v_mfma_f32_32x32x16_bf16 v[16:31], v[160:163], v[220:223], v[16:31]
	ds_read_b128 v[220:223], v224 offset:12288
	s_waitcnt lgkmcnt(3)
	v_mfma_f32_32x32x16_bf16 v[96:111], v[208:211], v[112:115], v[80:95]
	ds_read_b128 v[208:211], v225 offset:0
	s_waitcnt lgkmcnt(3)
	v_mfma_f32_32x32x16_bf16 v[80:95], v[212:215], v[112:115], v[80:95]
	ds_read_b128 v[212:215], v225 offset:12288
	s_waitcnt lgkmcnt(3)
	v_mfma_f32_32x32x16_bf16 v[96:111], v[216:219], v[116:119], v[96:111]
	ds_read_b128 v[216:219], v226 offset:0
	s_waitcnt lgkmcnt(3)
	v_mfma_f32_32x32x16_bf16 v[80:95], v[220:223], v[116:119], v[80:95]
	ds_read_b128 v[220:223], v226 offset:12288
	s_waitcnt lgkmcnt(3)
	v_mfma_f32_32x32x16_bf16 v[96:111], v[208:211], v[120:123], v[96:111]
	ds_read_b128 v[208:211], v207 offset:128
	s_waitcnt lgkmcnt(3)
	v_mfma_f32_32x32x16_bf16 v[80:95], v[212:215], v[120:123], v[80:95]
	ds_read_b128 v[212:215], v207 offset:12416
	s_waitcnt lgkmcnt(3)
	v_mfma_f32_32x32x16_bf16 v[96:111], v[216:219], v[124:127], v[96:111]
	ds_read_b128 v[216:219], v224 offset:128
	s_waitcnt lgkmcnt(3)
	v_mfma_f32_32x32x16_bf16 v[80:95], v[220:223], v[124:127], v[80:95]
	ds_read_b128 v[220:223], v224 offset:12416
	s_waitcnt lgkmcnt(3)
	v_mfma_f32_32x32x16_bf16 v[96:111], v[208:211], v[128:131], v[96:111]
	ds_read_b128 v[208:211], v225 offset:128
	s_waitcnt lgkmcnt(3)
	v_mfma_f32_32x32x16_bf16 v[80:95], v[212:215], v[128:131], v[80:95]
	ds_read_b128 v[212:215], v225 offset:12416
	s_waitcnt lgkmcnt(3)
	v_mfma_f32_32x32x16_bf16 v[96:111], v[216:219], v[132:135], v[96:111]
	ds_read_b128 v[216:219], v226 offset:128
	s_waitcnt lgkmcnt(3)
	v_mfma_f32_32x32x16_bf16 v[80:95], v[220:223], v[132:135], v[80:95]
	ds_read_b128 v[220:223], v226 offset:12416
	s_waitcnt lgkmcnt(3)
	v_mfma_f32_32x32x16_bf16 v[96:111], v[208:211], v[136:139], v[96:111]
	ds_read_b128 v[208:211], v207 offset:256
	s_waitcnt lgkmcnt(3)
	v_mfma_f32_32x32x16_bf16 v[80:95], v[212:215], v[136:139], v[80:95]
	ds_read_b128 v[212:215], v207 offset:12544
	s_waitcnt lgkmcnt(3)
	v_mfma_f32_32x32x16_bf16 v[96:111], v[216:219], v[140:143], v[96:111]
	ds_read_b128 v[216:219], v224 offset:256
	s_waitcnt lgkmcnt(3)
	v_mfma_f32_32x32x16_bf16 v[80:95], v[220:223], v[140:143], v[80:95]
	ds_read_b128 v[220:223], v224 offset:12544
	s_waitcnt lgkmcnt(3)
	v_mfma_f32_32x32x16_bf16 v[96:111], v[208:211], v[144:147], v[96:111]
	ds_read_b128 v[208:211], v225 offset:256
	s_waitcnt lgkmcnt(3)
	v_mfma_f32_32x32x16_bf16 v[80:95], v[212:215], v[144:147], v[80:95]
	ds_read_b128 v[212:215], v225 offset:12544
	s_waitcnt lgkmcnt(3)
	v_mfma_f32_32x32x16_bf16 v[96:111], v[216:219], v[148:151], v[96:111]
	ds_read_b128 v[216:219], v226 offset:256
	s_waitcnt lgkmcnt(3)
	v_mfma_f32_32x32x16_bf16 v[80:95], v[220:223], v[148:151], v[80:95]
	ds_read_b128 v[220:223], v226 offset:12544
	s_waitcnt lgkmcnt(3)
	v_mfma_f32_32x32x16_bf16 v[96:111], v[208:211], v[152:155], v[96:111]
	s_waitcnt lgkmcnt(2)
	v_mfma_f32_32x32x16_bf16 v[80:95], v[212:215], v[152:155], v[80:95]
	s_waitcnt lgkmcnt(1)
	v_mfma_f32_32x32x16_bf16 v[96:111], v[216:219], v[156:159], v[96:111]
	s_waitcnt lgkmcnt(0)
	v_mfma_f32_32x32x16_bf16 v[80:95], v[220:223], v[156:159], v[80:95]
	s_waitcnt vmcnt(0)
	s_waitcnt lgkmcnt(0)
	s_barrier
	s_add_u32 s44, s44, 0x18000
	s_addc_u32 s45, s45, 0
	v_lshl_add_u64 v[194:195], v[194:195], 0, s[28:29]
	s_cmp_eq_u32 s44, 0xbe8000
	v_lshl_add_u64 v[196:197], v[196:197], 0, s[28:29]
	s_cbranch_scc1 .LBB0_616
.LBB0_606:
	s_mul_i32 s46, s26, 0x6000
	s_addk_i32 s46, 0xa000
	s_cmp_lg_u32 s26, 0
	s_cselect_b32 s46, s46, 0xc000
	s_add_i32 s47, s26, 1
	s_cmp_lg_u32 s26, 2
	s_cselect_b32 s26, s47, 0
	s_lshl_b32 s93, s26, 14
	s_add_i32 s47, s76, s93
	s_cmp_eq_u32 s44, 0xbd0000
	s_cbranch_scc1 .LBB0_608
	s_add_u32 s98, s52, s44
	s_add_i32 m0, s46, s73
	s_addc_u32 s99, s53, s45
	global_load_lds_dwordx4 v178, s[98:99]
	s_add_i32 m0, s46, s74
	s_nop 0
	global_load_lds_dwordx4 v180, s[98:99]
	s_add_i32 m0, s46, s75
	s_nop 0
	global_load_lds_dwordx4 v182, s[98:99]
.LBB0_608:
	s_mov_b32 m0, s47
	v_max3_f32 v160, v96, v97, v80
	global_load_lds_dwordx4 v[194:195], off
	s_add_i32 m0, s47, 0x400
	v_max3_f32 v161, v98, v99, v81
	global_load_lds_dwordx4 v[196:197], off
	v_max3_f32 v160, v160, v82, v83
	v_max3_f32 v161, v161, v102, v103
	v_max3_f32 v160, v160, v100, v101
	v_max3_f32 v161, v161, v86, v87
	v_max3_f32 v160, v160, v84, v85
	v_max3_f32 v161, v161, v106, v107
	v_max3_f32 v160, v160, v104, v105
	v_max3_f32 v161, v161, v90, v91
	v_max3_f32 v160, v160, v88, v89
	v_max3_f32 v161, v161, v110, v111
	v_max3_f32 v160, v160, v108, v109
	v_max3_f32 v161, v161, v94, v95
	v_max3_f32 v160, v160, v92, v93
	v_max_f32 v160, v160, v161
	v_mov_b32_e32 v161, v160
	s_nop 0
	s_cmp_eq_u32 s44, 0
	v_permlane32_swap_b32_e32 v160, v161
	v_max_f32 v160, v160, v161
	s_cbranch_scc1 .LBB0_615
	v_cmp_lt_f32_e32 vcc, s87, v160
	s_cbranch_vccz .LBB0_605
	s_branch .LBB0_614
.LBB0_611:
	s_cmp_lg_u32 s44, 0
	s_cselect_b64 s[46:47], -1, 0
	s_andn2_b64 vcc, exec, s[46:47]
	s_cbranch_vccnz .LBB0_604
	v_exp_f32_e64 v161, -v160
	s_and_saveexec_b64 s[46:47], s[10:11]
	s_cbranch_execz .LBB0_603
	ds_write_b32 v201, v161 offset:128
	s_branch .LBB0_603

; __global__ void __launch_bounds__(512, 2) hymba_fwd(Args args) {
	.amdhsa_kernel _Z9hymba_fwd4Args
		.amdhsa_group_segment_fixed_size 0
		.amdhsa_private_segment_fixed_size 0
		.amdhsa_kernarg_size 472
		.amdhsa_user_sgpr_count 2
		.amdhsa_user_sgpr_dispatch_ptr 0
		.amdhsa_user_sgpr_queue_ptr 0
		.amdhsa_user_sgpr_kernarg_segment_ptr 1
		.amdhsa_user_sgpr_dispatch_id 0
		.amdhsa_user_sgpr_kernarg_preload_length 0
		.amdhsa_user_sgpr_kernarg_preload_offset 0
		.amdhsa_user_sgpr_private_segment_size 0
		.amdhsa_uses_dynamic_stack 0
		.amdhsa_enable_private_segment 0
		.amdhsa_system_sgpr_workgroup_id_x 1
		.amdhsa_system_sgpr_workgroup_id_y 0
		.amdhsa_system_sgpr_workgroup_id_z 0
		.amdhsa_system_sgpr_workgroup_info 0
		.amdhsa_system_vgpr_workitem_id 0
		.amdhsa_next_free_vgpr 249
		.amdhsa_next_free_sgpr 100
		.amdhsa_accum_offset 252
		.amdhsa_reserve_vcc 1
		.amdhsa_float_round_mode_32 0
		.amdhsa_float_round_mode_16_64 0
		.amdhsa_float_denorm_mode_32 3
		.amdhsa_float_denorm_mode_16_64 3
		.amdhsa_dx10_clamp 1
		.amdhsa_ieee_mode 1
		.amdhsa_fp16_overflow 0
		.amdhsa_tg_split 0
		.amdhsa_exception_fp_ieee_invalid_op 0
		.amdhsa_exception_fp_denorm_src 0
		.amdhsa_exception_fp_ieee_div_zero 0
		.amdhsa_exception_fp_ieee_overflow 0
		.amdhsa_exception_fp_ieee_underflow 0
		.amdhsa_exception_fp_ieee_inexact 0
		.amdhsa_exception_int_div_zero 0
	.end_amdhsa_kernel
